# fp8 GEMM steady loops: in the two light load sections (16 ds_read_b128 + 2 LDS-DMA) the DMA pieces and scalar bookkeeping are issued before the ds_read burst; on top of v5
# baseline (speedup 1.0000x reference)
.LBB0_388:
	s_add_u32 s44, s46, 0xfffe0080
	s_addc_u32 s45, s47, -1
	s_cmp_eq_u32 s75, 4
	s_cselect_b32 s49, s1, s45
	s_cselect_b32 s48, s5, s44
	s_cselect_b32 s45, s23, s74
	s_cselect_b32 s44, s26, s37
	s_mov_b32 m0, s27
	v_lshl_add_u64 v[224:225], s[46:47], 0, v[168:169]
	global_load_lds_dwordx4 v[224:225], off
	v_lshl_add_u64 v[224:225], s[46:47], 0, v[170:171]
	s_mov_b32 m0, s35
	s_nop 0
	global_load_lds_dwordx4 v[224:225], off
	ds_read_b128 v[2:5], v180
	ds_read_b128 v[6:9], v181
	ds_read_b128 v[10:13], v182
	ds_read_b128 v[14:17], v183
	ds_read_b128 v[26:29], v184
	ds_read_b128 v[30:33], v185
	ds_read_b128 v[172:175], v186
	ds_read_b128 v[176:179], v187
	ds_read_b128 v[18:21], v196
	ds_read_b128 v[22:25], v196 offset:1024
	ds_read_b128 v[198:201], v196 offset:2048
	ds_read_b128 v[202:205], v196 offset:3072
	ds_read_b128 v[206:209], v196 offset:4096
	ds_read_b128 v[210:213], v196 offset:5120
	ds_read_b128 v[216:219], v196 offset:6144
	ds_read_b128 v[220:223], v196 offset:7168
	s_waitcnt vmcnt(8)
	s_waitcnt lgkmcnt(0)
	s_barrier
	s_setprio 1
	s_waitcnt lgkmcnt(0)
	v_mfma_scale_f32_16x16x128_f8f6f4 v[158:161], v[2:9], v[18:25], v[158:161], v234, v235 op_sel_hi:[0,0,0]
	v_mfma_scale_f32_16x16x128_f8f6f4 v[154:157], v[10:17], v[18:25], v[154:157], v234, v235 op_sel_hi:[0,0,0]
	v_mfma_scale_f32_16x16x128_f8f6f4 v[150:153], v[2:9], v[198:205], v[150:153], v234, v235 op_sel_hi:[0,0,0]
	v_mfma_scale_f32_16x16x128_f8f6f4 v[146:149], v[10:17], v[198:205], v[146:149], v234, v235 op_sel_hi:[0,0,0]
	v_mfma_scale_f32_16x16x128_f8f6f4 v[142:145], v[2:9], v[206:213], v[142:145], v234, v235 op_sel_hi:[0,0,0]
	v_mfma_scale_f32_16x16x128_f8f6f4 v[138:141], v[10:17], v[206:213], v[138:141], v234, v235 op_sel_hi:[0,0,0]
	v_mfma_scale_f32_16x16x128_f8f6f4 v[134:137], v[2:9], v[216:223], v[134:137], v234, v235 op_sel_hi:[0,0,0]
	v_mfma_scale_f32_16x16x128_f8f6f4 v[130:133], v[10:17], v[216:223], v[130:133], v234, v235 op_sel_hi:[0,0,0]
	s_setprio 0
	s_setprio 1
	v_mfma_scale_f32_16x16x128_f8f6f4 v[126:129], v[26:33], v[18:25], v[126:129], v234, v235 op_sel_hi:[0,0,0]
	v_mfma_scale_f32_16x16x128_f8f6f4 v[122:125], v[172:179], v[18:25], v[122:125], v234, v235 op_sel_hi:[0,0,0]
	v_mfma_scale_f32_16x16x128_f8f6f4 v[118:121], v[26:33], v[198:205], v[118:121], v234, v235 op_sel_hi:[0,0,0]
	v_mfma_scale_f32_16x16x128_f8f6f4 v[114:117], v[172:179], v[198:205], v[114:117], v234, v235 op_sel_hi:[0,0,0]
	v_mfma_scale_f32_16x16x128_f8f6f4 v[110:113], v[26:33], v[206:213], v[110:113], v234, v235 op_sel_hi:[0,0,0]
	v_mfma_scale_f32_16x16x128_f8f6f4 v[106:109], v[172:179], v[206:213], v[106:109], v234, v235 op_sel_hi:[0,0,0]
	v_mfma_scale_f32_16x16x128_f8f6f4 v[102:105], v[26:33], v[216:223], v[102:105], v234, v235 op_sel_hi:[0,0,0]
	v_mfma_scale_f32_16x16x128_f8f6f4 v[98:101], v[172:179], v[216:223], v[98:101], v234, v235 op_sel_hi:[0,0,0]
	s_setprio 0
	s_barrier
	s_mov_b32 m0, s58
	v_lshl_add_u64 v[18:19], s[44:45], 0, v[0:1]
	s_add_u32 vcc_lo, s44, 0x20000
	ds_read_b128 v[198:201], v196 offset:16384
	ds_read_b128 v[202:205], v196 offset:17408
	ds_read_b128 v[206:209], v196 offset:18432
	ds_read_b128 v[210:213], v196 offset:19456
	ds_read_b128 v[216:219], v196 offset:20480
	ds_read_b128 v[220:223], v196 offset:21504
	ds_read_b128 v[224:227], v196 offset:22528
	ds_read_b128 v[228:231], v196 offset:23552
	global_load_lds_dwordx4 v[18:19], off
	v_lshl_add_u64 v[20:21], s[44:45], 0, v[166:167]
	s_mov_b32 m0, s59
	s_addc_u32 vcc_hi, s45, 0
	global_load_lds_dwordx4 v[20:21], off
	v_lshl_add_u64 v[22:23], vcc, 0, v[0:1]
	s_mov_b32 m0, s60
	v_lshl_add_u64 v[24:25], s[48:49], 0, v[164:165]
	global_load_lds_dwordx4 v[22:23], off
	v_lshl_add_u64 v[22:23], vcc, 0, v[166:167]
	s_mov_b32 m0, s61
	s_nop 0
	global_load_lds_dwordx4 v[22:23], off
	v_lshl_add_u64 v[22:23], s[48:49], 0, v[162:163]
	s_mov_b32 m0, s57
	s_nop 0
	global_load_lds_dwordx4 v[22:23], off
	s_mov_b32 m0, s62
	s_nop 0
	global_load_lds_dwordx4 v[24:25], off
	s_waitcnt vmcnt(8)
	s_waitcnt lgkmcnt(0)
	s_barrier
	s_setprio 1
	s_waitcnt lgkmcnt(0)
	v_mfma_scale_f32_16x16x128_f8f6f4 v[94:97], v[2:9], v[198:205], v[94:97], v234, v235 op_sel_hi:[0,0,0]
	v_mfma_scale_f32_16x16x128_f8f6f4 v[90:93], v[10:17], v[198:205], v[90:93], v234, v235 op_sel_hi:[0,0,0]
	v_mfma_scale_f32_16x16x128_f8f6f4 v[86:89], v[2:9], v[206:213], v[86:89], v234, v235 op_sel_hi:[0,0,0]
	v_mfma_scale_f32_16x16x128_f8f6f4 v[82:85], v[10:17], v[206:213], v[82:85], v234, v235 op_sel_hi:[0,0,0]
	v_mfma_scale_f32_16x16x128_f8f6f4 v[78:81], v[2:9], v[216:223], v[78:81], v234, v235 op_sel_hi:[0,0,0]
	v_mfma_scale_f32_16x16x128_f8f6f4 v[74:77], v[10:17], v[216:223], v[74:77], v234, v235 op_sel_hi:[0,0,0]
	v_mfma_scale_f32_16x16x128_f8f6f4 v[70:73], v[2:9], v[224:231], v[70:73], v234, v235 op_sel_hi:[0,0,0]
	v_mfma_scale_f32_16x16x128_f8f6f4 v[66:69], v[10:17], v[224:231], v[66:69], v234, v235 op_sel_hi:[0,0,0]
	s_setprio 0
	s_setprio 1
	v_mfma_scale_f32_16x16x128_f8f6f4 v[62:65], v[26:33], v[198:205], v[62:65], v234, v235 op_sel_hi:[0,0,0]
	v_mfma_scale_f32_16x16x128_f8f6f4 v[58:61], v[172:179], v[198:205], v[58:61], v234, v235 op_sel_hi:[0,0,0]
	v_mfma_scale_f32_16x16x128_f8f6f4 v[54:57], v[26:33], v[206:213], v[54:57], v234, v235 op_sel_hi:[0,0,0]
	v_mfma_scale_f32_16x16x128_f8f6f4 v[50:53], v[172:179], v[206:213], v[50:53], v234, v235 op_sel_hi:[0,0,0]
	v_mfma_scale_f32_16x16x128_f8f6f4 v[46:49], v[26:33], v[216:223], v[46:49], v234, v235 op_sel_hi:[0,0,0]
	v_mfma_scale_f32_16x16x128_f8f6f4 v[42:45], v[172:179], v[216:223], v[42:45], v234, v235 op_sel_hi:[0,0,0]
	v_mfma_scale_f32_16x16x128_f8f6f4 v[38:41], v[26:33], v[224:231], v[38:41], v234, v235 op_sel_hi:[0,0,0]
	v_mfma_scale_f32_16x16x128_f8f6f4 v[34:37], v[172:179], v[224:231], v[34:37], v234, v235 op_sel_hi:[0,0,0]
	s_setprio 0
	s_barrier
	s_add_u32 s48, s48, 0x20000
	s_addc_u32 s49, s49, 0
	s_mov_b32 m0, s63
	v_lshl_add_u64 v[232:233], s[48:49], 0, v[162:163]
	global_load_lds_dwordx4 v[232:233], off
	v_lshl_add_u64 v[232:233], s[48:49], 0, v[164:165]
	s_mov_b32 m0, s64
	s_nop 0
	global_load_lds_dwordx4 v[232:233], off
	ds_read_b128 v[10:13], v188
	ds_read_b128 v[14:17], v189
	ds_read_b128 v[26:29], v190
	ds_read_b128 v[30:33], v191
	ds_read_b128 v[2:5], v192
	ds_read_b128 v[6:9], v193
	ds_read_b128 v[172:175], v194
	ds_read_b128 v[176:179], v195
	ds_read_b128 v[198:201], v196 offset:32768
	ds_read_b128 v[202:205], v196 offset:33792
	ds_read_b128 v[206:209], v196 offset:34816
	ds_read_b128 v[210:213], v196 offset:35840
	ds_read_b128 v[216:219], v196 offset:36864
	ds_read_b128 v[220:223], v196 offset:37888
	ds_read_b128 v[224:227], v196 offset:38912
	ds_read_b128 v[228:231], v196 offset:39936
	s_waitcnt vmcnt(8)
	s_waitcnt lgkmcnt(0)
	s_barrier
	s_setprio 1
	s_waitcnt lgkmcnt(0)
	v_mfma_scale_f32_16x16x128_f8f6f4 v[158:161], v[10:17], v[198:205], v[158:161], v234, v235 op_sel_hi:[0,0,0]
	v_mfma_scale_f32_16x16x128_f8f6f4 v[154:157], v[26:33], v[198:205], v[154:157], v234, v235 op_sel_hi:[0,0,0]
	v_mfma_scale_f32_16x16x128_f8f6f4 v[150:153], v[10:17], v[206:213], v[150:153], v234, v235 op_sel_hi:[0,0,0]
	v_mfma_scale_f32_16x16x128_f8f6f4 v[146:149], v[26:33], v[206:213], v[146:149], v234, v235 op_sel_hi:[0,0,0]
	v_mfma_scale_f32_16x16x128_f8f6f4 v[142:145], v[10:17], v[216:223], v[142:145], v234, v235 op_sel_hi:[0,0,0]
	v_mfma_scale_f32_16x16x128_f8f6f4 v[138:141], v[26:33], v[216:223], v[138:141], v234, v235 op_sel_hi:[0,0,0]
	v_mfma_scale_f32_16x16x128_f8f6f4 v[134:137], v[10:17], v[224:231], v[134:137], v234, v235 op_sel_hi:[0,0,0]
	v_mfma_scale_f32_16x16x128_f8f6f4 v[130:133], v[26:33], v[224:231], v[130:133], v234, v235 op_sel_hi:[0,0,0]
	s_setprio 0
	s_setprio 1
	v_mfma_scale_f32_16x16x128_f8f6f4 v[126:129], v[2:9], v[198:205], v[126:129], v234, v235 op_sel_hi:[0,0,0]
	v_mfma_scale_f32_16x16x128_f8f6f4 v[122:125], v[172:179], v[198:205], v[122:125], v234, v235 op_sel_hi:[0,0,0]
	v_mfma_scale_f32_16x16x128_f8f6f4 v[118:121], v[2:9], v[206:213], v[118:121], v234, v235 op_sel_hi:[0,0,0]
	v_mfma_scale_f32_16x16x128_f8f6f4 v[114:117], v[172:179], v[206:213], v[114:117], v234, v235 op_sel_hi:[0,0,0]
	v_mfma_scale_f32_16x16x128_f8f6f4 v[110:113], v[2:9], v[216:223], v[110:113], v234, v235 op_sel_hi:[0,0,0]
	v_mfma_scale_f32_16x16x128_f8f6f4 v[106:109], v[172:179], v[216:223], v[106:109], v234, v235 op_sel_hi:[0,0,0]
	v_mfma_scale_f32_16x16x128_f8f6f4 v[102:105], v[2:9], v[224:231], v[102:105], v234, v235 op_sel_hi:[0,0,0]
	v_mfma_scale_f32_16x16x128_f8f6f4 v[98:101], v[172:179], v[224:231], v[98:101], v234, v235 op_sel_hi:[0,0,0]
	s_setprio 0
	s_barrier
	s_mov_b32 m0, s7
	v_lshl_add_u64 v[18:19], v[18:19], 0, s[66:67]
	s_add_u32 s44, s44, 0x20080
	ds_read_b128 v[198:201], v196 offset:49152
	ds_read_b128 v[202:205], v196 offset:50176
	ds_read_b128 v[206:209], v196 offset:51200
	ds_read_b128 v[210:213], v196 offset:52224
	ds_read_b128 v[216:219], v196 offset:53248
	ds_read_b128 v[220:223], v196 offset:54272
	ds_read_b128 v[224:227], v196 offset:55296
	ds_read_b128 v[228:231], v196 offset:56320
	global_load_lds_dwordx4 v[18:19], off
	v_lshl_add_u64 v[18:19], v[20:21], 0, s[66:67]
	s_mov_b32 m0, s65
	s_addc_u32 s45, s45, 0
	global_load_lds_dwordx4 v[18:19], off
	v_lshl_add_u64 v[18:19], s[44:45], 0, v[0:1]
	s_mov_b32 m0, s13
	s_nop 0
	global_load_lds_dwordx4 v[18:19], off
	v_lshl_add_u64 v[18:19], s[44:45], 0, v[166:167]
	s_mov_b32 m0, s51
	s_nop 0
	global_load_lds_dwordx4 v[18:19], off
	v_lshl_add_u64 v[18:19], v[22:23], 0, s[66:67]
	s_mov_b32 m0, s68
	s_nop 0
	global_load_lds_dwordx4 v[18:19], off
	v_lshl_add_u64 v[18:19], v[24:25], 0, s[66:67]
	s_mov_b32 m0, s52
	s_nop 0
	global_load_lds_dwordx4 v[18:19], off
	s_waitcnt vmcnt(8)
	s_waitcnt lgkmcnt(0)
	s_barrier
	s_setprio 1
	s_waitcnt lgkmcnt(0)
	v_mfma_scale_f32_16x16x128_f8f6f4 v[94:97], v[10:17], v[198:205], v[94:97], v234, v235 op_sel_hi:[0,0,0]
	v_mfma_scale_f32_16x16x128_f8f6f4 v[90:93], v[26:33], v[198:205], v[90:93], v234, v235 op_sel_hi:[0,0,0]
	v_mfma_scale_f32_16x16x128_f8f6f4 v[86:89], v[10:17], v[206:213], v[86:89], v234, v235 op_sel_hi:[0,0,0]
	v_mfma_scale_f32_16x16x128_f8f6f4 v[82:85], v[26:33], v[206:213], v[82:85], v234, v235 op_sel_hi:[0,0,0]
	v_mfma_scale_f32_16x16x128_f8f6f4 v[78:81], v[10:17], v[216:223], v[78:81], v234, v235 op_sel_hi:[0,0,0]
	v_mfma_scale_f32_16x16x128_f8f6f4 v[74:77], v[26:33], v[216:223], v[74:77], v234, v235 op_sel_hi:[0,0,0]
	v_mfma_scale_f32_16x16x128_f8f6f4 v[70:73], v[10:17], v[224:231], v[70:73], v234, v235 op_sel_hi:[0,0,0]
	v_mfma_scale_f32_16x16x128_f8f6f4 v[66:69], v[26:33], v[224:231], v[66:69], v234, v235 op_sel_hi:[0,0,0]
	s_setprio 0
	s_setprio 1
	v_mfma_scale_f32_16x16x128_f8f6f4 v[62:65], v[2:9], v[198:205], v[62:65], v234, v235 op_sel_hi:[0,0,0]
	v_mfma_scale_f32_16x16x128_f8f6f4 v[58:61], v[172:179], v[198:205], v[58:61], v234, v235 op_sel_hi:[0,0,0]
	v_mfma_scale_f32_16x16x128_f8f6f4 v[54:57], v[2:9], v[206:213], v[54:57], v234, v235 op_sel_hi:[0,0,0]
	v_mfma_scale_f32_16x16x128_f8f6f4 v[50:53], v[172:179], v[206:213], v[50:53], v234, v235 op_sel_hi:[0,0,0]
	v_mfma_scale_f32_16x16x128_f8f6f4 v[46:49], v[2:9], v[216:223], v[46:49], v234, v235 op_sel_hi:[0,0,0]
	v_mfma_scale_f32_16x16x128_f8f6f4 v[42:45], v[172:179], v[216:223], v[42:45], v234, v235 op_sel_hi:[0,0,0]
	v_mfma_scale_f32_16x16x128_f8f6f4 v[38:41], v[2:9], v[224:231], v[38:41], v234, v235 op_sel_hi:[0,0,0]
	v_mfma_scale_f32_16x16x128_f8f6f4 v[34:37], v[172:179], v[224:231], v[34:37], v234, v235 op_sel_hi:[0,0,0]
	s_setprio 0
	s_barrier
	s_add_i32 s75, s75, 2
	s_add_u32 s46, s46, 0x100
	s_addc_u32 s47, s47, 0
	s_add_u32 s37, s37, 0x100
	s_addc_u32 s74, s74, 0
	s_cmp_gt_u32 s75, 5
	s_cbranch_scc0 .LBB0_388
	s_and_b64 vcc, exec, s[30:31]
	s_cbranch_vccz .LBB0_391
	s_barrier

.LBB0_2002:
	s_add_u32 s58, s54, 0x80
	s_addc_u32 s59, s55, 0
	s_and_b64 s[56:57], s[4:5], exec
	s_cselect_b32 s59, s9, s59
	s_cselect_b32 s58, s8, s58
	s_cselect_b32 s57, s47, s45
	s_cselect_b32 s56, s46, s43
	s_mov_b32 m0, s27
	v_lshl_add_u64 v[170:171], s[54:55], 0, v[166:167]
	global_load_lds_dwordx4 v[170:171], off
	v_lshl_add_u64 v[170:171], s[54:55], 0, v[168:169]
	s_mov_b32 m0, s41
	s_nop 0
	global_load_lds_dwordx4 v[170:171], off
	ds_read_b128 v[2:5], v183
	ds_read_b128 v[6:9], v182
	ds_read_b128 v[10:13], v181
	ds_read_b128 v[14:17], v180
	ds_read_b128 v[26:29], v179
	ds_read_b128 v[30:33], v178
	ds_read_b128 v[198:201], v177
	ds_read_b128 v[202:205], v176
	ds_read_b128 v[18:21], v192
	ds_read_b128 v[22:25], v192 offset:1024
	ds_read_b128 v[206:209], v192 offset:2048
	ds_read_b128 v[210:213], v192 offset:3072
	ds_read_b128 v[216:219], v192 offset:4096
	ds_read_b128 v[220:223], v192 offset:5120
	ds_read_b128 v[224:227], v192 offset:6144
	ds_read_b128 v[228:231], v192 offset:7168
	s_waitcnt vmcnt(8)
	s_waitcnt lgkmcnt(0)
	s_barrier
	s_setprio 1
	s_waitcnt lgkmcnt(0)
	v_mfma_scale_f32_16x16x128_f8f6f4 v[150:153], v[2:9], v[18:25], v[150:153], v234, v235 op_sel_hi:[0,0,0]
	v_mfma_scale_f32_16x16x128_f8f6f4 v[146:149], v[10:17], v[18:25], v[146:149], v234, v235 op_sel_hi:[0,0,0]
	v_mfma_scale_f32_16x16x128_f8f6f4 v[142:145], v[2:9], v[206:213], v[142:145], v234, v235 op_sel_hi:[0,0,0]
	v_mfma_scale_f32_16x16x128_f8f6f4 v[138:141], v[10:17], v[206:213], v[138:141], v234, v235 op_sel_hi:[0,0,0]
	v_mfma_scale_f32_16x16x128_f8f6f4 v[134:137], v[2:9], v[216:223], v[134:137], v234, v235 op_sel_hi:[0,0,0]
	v_mfma_scale_f32_16x16x128_f8f6f4 v[130:133], v[10:17], v[216:223], v[130:133], v234, v235 op_sel_hi:[0,0,0]
	v_mfma_scale_f32_16x16x128_f8f6f4 v[126:129], v[2:9], v[224:231], v[126:129], v234, v235 op_sel_hi:[0,0,0]
	v_mfma_scale_f32_16x16x128_f8f6f4 v[122:125], v[10:17], v[224:231], v[122:125], v234, v235 op_sel_hi:[0,0,0]
	s_setprio 0
	s_setprio 1
	v_mfma_scale_f32_16x16x128_f8f6f4 v[118:121], v[26:33], v[18:25], v[118:121], v234, v235 op_sel_hi:[0,0,0]
	v_mfma_scale_f32_16x16x128_f8f6f4 v[114:117], v[198:205], v[18:25], v[114:117], v234, v235 op_sel_hi:[0,0,0]
	v_mfma_scale_f32_16x16x128_f8f6f4 v[110:113], v[26:33], v[206:213], v[110:113], v234, v235 op_sel_hi:[0,0,0]
	v_mfma_scale_f32_16x16x128_f8f6f4 v[106:109], v[198:205], v[206:213], v[106:109], v234, v235 op_sel_hi:[0,0,0]
	v_mfma_scale_f32_16x16x128_f8f6f4 v[102:105], v[26:33], v[216:223], v[102:105], v234, v235 op_sel_hi:[0,0,0]
	v_mfma_scale_f32_16x16x128_f8f6f4 v[98:101], v[198:205], v[216:223], v[98:101], v234, v235 op_sel_hi:[0,0,0]
	v_mfma_scale_f32_16x16x128_f8f6f4 v[94:97], v[26:33], v[224:231], v[94:97], v234, v235 op_sel_hi:[0,0,0]
	v_mfma_scale_f32_16x16x128_f8f6f4 v[90:93], v[198:205], v[224:231], v[90:93], v234, v235 op_sel_hi:[0,0,0]
	s_setprio 0
	s_barrier
	s_mov_b32 m0, s68
	v_lshl_add_u64 v[18:19], s[56:57], 0, v[162:163]
	s_add_u32 vcc_lo, s56, 0x20000
	ds_read_b128 v[206:209], v192 offset:16384
	ds_read_b128 v[210:213], v192 offset:17408
	ds_read_b128 v[216:219], v192 offset:18432
	ds_read_b128 v[220:223], v192 offset:19456
	ds_read_b128 v[224:227], v192 offset:20480
	ds_read_b128 v[228:231], v192 offset:21504
	ds_read_b128 v[244:247], v192 offset:22528
	ds_read_b128 v[248:251], v192 offset:23552
	global_load_lds_dwordx4 v[18:19], off
	v_lshl_add_u64 v[20:21], s[56:57], 0, v[164:165]
	s_mov_b32 m0, s60
	s_addc_u32 vcc_hi, s57, 0
	global_load_lds_dwordx4 v[20:21], off
	v_lshl_add_u64 v[22:23], vcc, 0, v[162:163]
	s_mov_b32 m0, s61
	s_nop 0
	global_load_lds_dwordx4 v[22:23], off
	v_lshl_add_u64 v[22:23], vcc, 0, v[164:165]
	s_mov_b32 m0, s62
	s_nop 0
	global_load_lds_dwordx4 v[22:23], off
	v_cndmask_b32_e64 v22, v195, v193, s[4:5]
	v_lshlrev_b32_e32 v0, 10, v22
	v_and_or_b32 v0, v0, s82, v174
	v_bfe_u32 v22, v22, 16, 16
	s_mov_b32 m0, s65
	v_lshl_add_u32 v22, v22, 10, v175
	global_load_lds_dwordx4 v0, s[58:59]
	s_mov_b32 m0, s63
	v_mov_b32_e32 v23, v1
	global_load_lds_dwordx4 v22, s[58:59]
	s_waitcnt vmcnt(8)
	s_waitcnt lgkmcnt(0)
	v_lshl_add_u64 v[24:25], s[58:59], 0, v[0:1]
	v_lshl_add_u64 v[22:23], s[58:59], 0, v[22:23]
	s_barrier
	s_setprio 1
	s_waitcnt lgkmcnt(0)
	v_mfma_scale_f32_16x16x128_f8f6f4 v[86:89], v[2:9], v[206:213], v[86:89], v234, v235 op_sel_hi:[0,0,0]
	v_mfma_scale_f32_16x16x128_f8f6f4 v[82:85], v[10:17], v[206:213], v[82:85], v234, v235 op_sel_hi:[0,0,0]
	v_mfma_scale_f32_16x16x128_f8f6f4 v[78:81], v[2:9], v[216:223], v[78:81], v234, v235 op_sel_hi:[0,0,0]
	v_mfma_scale_f32_16x16x128_f8f6f4 v[74:77], v[10:17], v[216:223], v[74:77], v234, v235 op_sel_hi:[0,0,0]
	v_mfma_scale_f32_16x16x128_f8f6f4 v[70:73], v[2:9], v[224:231], v[70:73], v234, v235 op_sel_hi:[0,0,0]
	v_mfma_scale_f32_16x16x128_f8f6f4 v[66:69], v[10:17], v[224:231], v[66:69], v234, v235 op_sel_hi:[0,0,0]
	v_mfma_scale_f32_16x16x128_f8f6f4 v[62:65], v[2:9], v[244:251], v[62:65], v234, v235 op_sel_hi:[0,0,0]
	v_mfma_scale_f32_16x16x128_f8f6f4 v[58:61], v[10:17], v[244:251], v[58:61], v234, v235 op_sel_hi:[0,0,0]
	s_setprio 0
	s_setprio 1
	v_mfma_scale_f32_16x16x128_f8f6f4 v[54:57], v[26:33], v[206:213], v[54:57], v234, v235 op_sel_hi:[0,0,0]
	v_mfma_scale_f32_16x16x128_f8f6f4 v[50:53], v[198:205], v[206:213], v[50:53], v234, v235 op_sel_hi:[0,0,0]
	v_mfma_scale_f32_16x16x128_f8f6f4 v[46:49], v[26:33], v[216:223], v[46:49], v234, v235 op_sel_hi:[0,0,0]
	v_mfma_scale_f32_16x16x128_f8f6f4 v[42:45], v[198:205], v[216:223], v[42:45], v234, v235 op_sel_hi:[0,0,0]
	v_mfma_scale_f32_16x16x128_f8f6f4 v[38:41], v[26:33], v[224:231], v[38:41], v234, v235 op_sel_hi:[0,0,0]
	v_mfma_scale_f32_16x16x128_f8f6f4 v[34:37], v[198:205], v[224:231], v[34:37], v234, v235 op_sel_hi:[0,0,0]
	v_mfma_scale_f32_16x16x128_f8f6f4 v[154:157], v[26:33], v[244:251], v[154:157], v234, v235 op_sel_hi:[0,0,0]
	v_mfma_scale_f32_16x16x128_f8f6f4 v[158:161], v[198:205], v[244:251], v[158:161], v234, v235 op_sel_hi:[0,0,0]
	s_setprio 0
	s_barrier
	v_cndmask_b32_e64 v0, v196, v194, s[4:5]
	v_lshlrev_b32_e32 v170, 10, v0
	s_mov_b32 m0, s10
	v_and_or_b32 v170, v170, s82, v174
	v_bfe_u32 v0, v0, 16, 16
	v_lshl_add_u32 v0, v0, 10, v175
	global_load_lds_dwordx4 v170, s[58:59]
	s_mov_b32 m0, s11
	s_nop 0
	global_load_lds_dwordx4 v0, s[58:59]
	ds_read_b128 v[10:13], v184
	ds_read_b128 v[14:17], v185
	ds_read_b128 v[26:29], v186
	ds_read_b128 v[30:33], v187
	ds_read_b128 v[2:5], v188
	ds_read_b128 v[6:9], v189
	ds_read_b128 v[198:201], v190
	ds_read_b128 v[202:205], v191
	ds_read_b128 v[206:209], v192 offset:32768
	ds_read_b128 v[210:213], v192 offset:33792
	ds_read_b128 v[216:219], v192 offset:34816
	ds_read_b128 v[220:223], v192 offset:35840
	ds_read_b128 v[224:227], v192 offset:36864
	ds_read_b128 v[228:231], v192 offset:37888
	ds_read_b128 v[244:247], v192 offset:38912
	ds_read_b128 v[248:251], v192 offset:39936
	s_waitcnt vmcnt(8)
	s_waitcnt lgkmcnt(0)
	s_barrier
	s_setprio 1
	s_waitcnt lgkmcnt(0)
	v_mfma_scale_f32_16x16x128_f8f6f4 v[150:153], v[10:17], v[206:213], v[150:153], v234, v235 op_sel_hi:[0,0,0]
	v_mfma_scale_f32_16x16x128_f8f6f4 v[146:149], v[26:33], v[206:213], v[146:149], v234, v235 op_sel_hi:[0,0,0]
	v_mfma_scale_f32_16x16x128_f8f6f4 v[142:145], v[10:17], v[216:223], v[142:145], v234, v235 op_sel_hi:[0,0,0]
	v_mfma_scale_f32_16x16x128_f8f6f4 v[138:141], v[26:33], v[216:223], v[138:141], v234, v235 op_sel_hi:[0,0,0]
	v_mfma_scale_f32_16x16x128_f8f6f4 v[134:137], v[10:17], v[224:231], v[134:137], v234, v235 op_sel_hi:[0,0,0]
	v_mfma_scale_f32_16x16x128_f8f6f4 v[130:133], v[26:33], v[224:231], v[130:133], v234, v235 op_sel_hi:[0,0,0]
	v_mfma_scale_f32_16x16x128_f8f6f4 v[126:129], v[10:17], v[244:251], v[126:129], v234, v235 op_sel_hi:[0,0,0]
	v_mfma_scale_f32_16x16x128_f8f6f4 v[122:125], v[26:33], v[244:251], v[122:125], v234, v235 op_sel_hi:[0,0,0]
	s_setprio 0
	s_setprio 1
	v_mfma_scale_f32_16x16x128_f8f6f4 v[118:121], v[2:9], v[206:213], v[118:121], v234, v235 op_sel_hi:[0,0,0]
	v_mfma_scale_f32_16x16x128_f8f6f4 v[114:117], v[198:205], v[206:213], v[114:117], v234, v235 op_sel_hi:[0,0,0]
	v_mfma_scale_f32_16x16x128_f8f6f4 v[110:113], v[2:9], v[216:223], v[110:113], v234, v235 op_sel_hi:[0,0,0]
	v_mfma_scale_f32_16x16x128_f8f6f4 v[106:109], v[198:205], v[216:223], v[106:109], v234, v235 op_sel_hi:[0,0,0]
	v_mfma_scale_f32_16x16x128_f8f6f4 v[102:105], v[2:9], v[224:231], v[102:105], v234, v235 op_sel_hi:[0,0,0]
	v_mfma_scale_f32_16x16x128_f8f6f4 v[98:101], v[198:205], v[224:231], v[98:101], v234, v235 op_sel_hi:[0,0,0]
	v_mfma_scale_f32_16x16x128_f8f6f4 v[94:97], v[2:9], v[244:251], v[94:97], v234, v235 op_sel_hi:[0,0,0]
	v_mfma_scale_f32_16x16x128_f8f6f4 v[90:93], v[198:205], v[244:251], v[90:93], v234, v235 op_sel_hi:[0,0,0]
	s_setprio 0
	s_barrier
	s_mov_b32 m0, s64
	v_lshl_add_u64 v[18:19], v[18:19], 0, s[66:67]
	s_add_u32 s4, s56, 0x20080
	ds_read_b128 v[206:209], v192 offset:49152
	ds_read_b128 v[210:213], v192 offset:50176
	ds_read_b128 v[216:219], v192 offset:51200
	ds_read_b128 v[220:223], v192 offset:52224
	ds_read_b128 v[224:227], v192 offset:53248
	ds_read_b128 v[228:231], v192 offset:54272
	ds_read_b128 v[244:247], v192 offset:55296
	ds_read_b128 v[248:251], v192 offset:56320
	global_load_lds_dwordx4 v[18:19], off
	v_lshl_add_u64 v[18:19], v[20:21], 0, s[66:67]
	s_mov_b32 m0, s81
	s_addc_u32 s5, s57, 0
	global_load_lds_dwordx4 v[18:19], off
	v_lshl_add_u64 v[18:19], s[4:5], 0, v[162:163]
	s_mov_b32 m0, s49
	s_nop 0
	global_load_lds_dwordx4 v[18:19], off
	v_lshl_add_u64 v[18:19], s[4:5], 0, v[164:165]
	s_mov_b32 m0, s30
	s_nop 0
	global_load_lds_dwordx4 v[18:19], off
	v_lshl_add_u64 v[18:19], v[24:25], 0, s[66:67]
	s_mov_b32 m0, s6
	s_nop 0
	global_load_lds_dwordx4 v[18:19], off
	v_lshl_add_u64 v[18:19], v[22:23], 0, s[66:67]
	s_mov_b32 m0, s7
	s_nop 0
	global_load_lds_dwordx4 v[18:19], off
	s_waitcnt vmcnt(8)
	s_waitcnt lgkmcnt(0)
	s_barrier
	s_setprio 1
	s_waitcnt lgkmcnt(0)
	v_mfma_scale_f32_16x16x128_f8f6f4 v[86:89], v[10:17], v[206:213], v[86:89], v234, v235 op_sel_hi:[0,0,0]
	v_mfma_scale_f32_16x16x128_f8f6f4 v[82:85], v[26:33], v[206:213], v[82:85], v234, v235 op_sel_hi:[0,0,0]
	v_mfma_scale_f32_16x16x128_f8f6f4 v[78:81], v[10:17], v[216:223], v[78:81], v234, v235 op_sel_hi:[0,0,0]
	v_mfma_scale_f32_16x16x128_f8f6f4 v[74:77], v[26:33], v[216:223], v[74:77], v234, v235 op_sel_hi:[0,0,0]
	v_mfma_scale_f32_16x16x128_f8f6f4 v[70:73], v[10:17], v[224:231], v[70:73], v234, v235 op_sel_hi:[0,0,0]
	v_mfma_scale_f32_16x16x128_f8f6f4 v[66:69], v[26:33], v[224:231], v[66:69], v234, v235 op_sel_hi:[0,0,0]
	v_mfma_scale_f32_16x16x128_f8f6f4 v[62:65], v[10:17], v[244:251], v[62:65], v234, v235 op_sel_hi:[0,0,0]
	v_mfma_scale_f32_16x16x128_f8f6f4 v[58:61], v[26:33], v[244:251], v[58:61], v234, v235 op_sel_hi:[0,0,0]
	s_setprio 0
	s_setprio 1
	v_mfma_scale_f32_16x16x128_f8f6f4 v[54:57], v[2:9], v[206:213], v[54:57], v234, v235 op_sel_hi:[0,0,0]
	v_mfma_scale_f32_16x16x128_f8f6f4 v[50:53], v[198:205], v[206:213], v[50:53], v234, v235 op_sel_hi:[0,0,0]
	v_mfma_scale_f32_16x16x128_f8f6f4 v[46:49], v[2:9], v[216:223], v[46:49], v234, v235 op_sel_hi:[0,0,0]
	v_mfma_scale_f32_16x16x128_f8f6f4 v[42:45], v[198:205], v[216:223], v[42:45], v234, v235 op_sel_hi:[0,0,0]
	v_mfma_scale_f32_16x16x128_f8f6f4 v[38:41], v[2:9], v[224:231], v[38:41], v234, v235 op_sel_hi:[0,0,0]
	v_mfma_scale_f32_16x16x128_f8f6f4 v[34:37], v[198:205], v[224:231], v[34:37], v234, v235 op_sel_hi:[0,0,0]
	v_mfma_scale_f32_16x16x128_f8f6f4 v[154:157], v[2:9], v[244:251], v[154:157], v234, v235 op_sel_hi:[0,0,0]
	v_mfma_scale_f32_16x16x128_f8f6f4 v[158:161], v[198:205], v[244:251], v[158:161], v234, v235 op_sel_hi:[0,0,0]
	s_setprio 0
	s_barrier
	s_add_i32 s74, s74, 2
	s_add_u32 s54, s54, 0x100
	s_addc_u32 s55, s55, 0
	s_add_u32 s43, s43, 0x100
	s_addc_u32 s45, s45, 0
	s_cmp_gt_u32 s74, 5
	s_cbranch_scc1 .LBB0_2005

.LBB0_2089:
	s_add_u32 s44, s42, 0xfffe0080
	s_addc_u32 s45, s43, -1
	s_cmp_eq_u32 s74, 4
	s_cselect_b32 s47, s13, s45
	s_cselect_b32 s46, s27, s44
	s_cselect_b32 s45, s35, s49
	s_cselect_b32 s44, s34, s48
	s_mov_b32 m0, s29
	v_lshl_add_u64 v[224:225], s[42:43], 0, v[168:169]
	global_load_lds_dwordx4 v[224:225], off
	v_lshl_add_u64 v[224:225], s[42:43], 0, v[170:171]
	s_mov_b32 m0, s31
	s_nop 0
	global_load_lds_dwordx4 v[224:225], off
	ds_read_b128 v[2:5], v180
	ds_read_b128 v[6:9], v181
	ds_read_b128 v[10:13], v182
	ds_read_b128 v[14:17], v183
	ds_read_b128 v[26:29], v184
	ds_read_b128 v[30:33], v185
	ds_read_b128 v[172:175], v186
	ds_read_b128 v[176:179], v187
	ds_read_b128 v[18:21], v196
	ds_read_b128 v[22:25], v196 offset:1024
	ds_read_b128 v[198:201], v196 offset:2048
	ds_read_b128 v[202:205], v196 offset:3072
	ds_read_b128 v[206:209], v196 offset:4096
	ds_read_b128 v[210:213], v196 offset:5120
	ds_read_b128 v[216:219], v196 offset:6144
	ds_read_b128 v[220:223], v196 offset:7168
	s_waitcnt vmcnt(8)
	s_waitcnt lgkmcnt(0)
	s_barrier
	s_setprio 1
	s_waitcnt lgkmcnt(0)
	v_mfma_scale_f32_16x16x128_f8f6f4 v[158:161], v[2:9], v[18:25], v[158:161], v234, v238 op_sel_hi:[0,0,0]
	v_mfma_scale_f32_16x16x128_f8f6f4 v[154:157], v[10:17], v[18:25], v[154:157], v234, v238 op_sel_hi:[0,0,0]
	v_mfma_scale_f32_16x16x128_f8f6f4 v[150:153], v[2:9], v[198:205], v[150:153], v234, v238 op_sel_hi:[0,0,0]
	v_mfma_scale_f32_16x16x128_f8f6f4 v[146:149], v[10:17], v[198:205], v[146:149], v234, v238 op_sel_hi:[0,0,0]
	v_mfma_scale_f32_16x16x128_f8f6f4 v[142:145], v[2:9], v[206:213], v[142:145], v234, v238 op_sel_hi:[0,0,0]
	v_mfma_scale_f32_16x16x128_f8f6f4 v[138:141], v[10:17], v[206:213], v[138:141], v234, v238 op_sel_hi:[0,0,0]
	v_mfma_scale_f32_16x16x128_f8f6f4 v[134:137], v[2:9], v[216:223], v[134:137], v234, v238 op_sel_hi:[0,0,0]
	v_mfma_scale_f32_16x16x128_f8f6f4 v[130:133], v[10:17], v[216:223], v[130:133], v234, v238 op_sel_hi:[0,0,0]
	s_setprio 0
	s_setprio 1
	v_mfma_scale_f32_16x16x128_f8f6f4 v[126:129], v[26:33], v[18:25], v[126:129], v234, v238 op_sel_hi:[0,0,0]
	v_mfma_scale_f32_16x16x128_f8f6f4 v[122:125], v[172:179], v[18:25], v[122:125], v234, v238 op_sel_hi:[0,0,0]
	v_mfma_scale_f32_16x16x128_f8f6f4 v[118:121], v[26:33], v[198:205], v[118:121], v234, v238 op_sel_hi:[0,0,0]
	v_mfma_scale_f32_16x16x128_f8f6f4 v[114:117], v[172:179], v[198:205], v[114:117], v234, v238 op_sel_hi:[0,0,0]
	v_mfma_scale_f32_16x16x128_f8f6f4 v[110:113], v[26:33], v[206:213], v[110:113], v234, v238 op_sel_hi:[0,0,0]
	v_mfma_scale_f32_16x16x128_f8f6f4 v[106:109], v[172:179], v[206:213], v[106:109], v234, v238 op_sel_hi:[0,0,0]
	v_mfma_scale_f32_16x16x128_f8f6f4 v[102:105], v[26:33], v[216:223], v[102:105], v234, v238 op_sel_hi:[0,0,0]
	v_mfma_scale_f32_16x16x128_f8f6f4 v[98:101], v[172:179], v[216:223], v[98:101], v234, v238 op_sel_hi:[0,0,0]
	s_setprio 0
	s_barrier
	s_mov_b32 m0, s41
	v_lshl_add_u64 v[18:19], s[44:45], 0, v[0:1]
	s_add_u32 vcc_lo, s44, 0x20000
	ds_read_b128 v[198:201], v196 offset:16384
	ds_read_b128 v[202:205], v196 offset:17408
	ds_read_b128 v[206:209], v196 offset:18432
	ds_read_b128 v[210:213], v196 offset:19456
	ds_read_b128 v[216:219], v196 offset:20480
	ds_read_b128 v[220:223], v196 offset:21504
	ds_read_b128 v[224:227], v196 offset:22528
	ds_read_b128 v[228:231], v196 offset:23552
	global_load_lds_dwordx4 v[18:19], off
	v_lshl_add_u64 v[20:21], s[44:45], 0, v[166:167]
	s_mov_b32 m0, s57
	s_addc_u32 vcc_hi, s45, 0
	global_load_lds_dwordx4 v[20:21], off
	v_lshl_add_u64 v[22:23], vcc, 0, v[0:1]
	s_mov_b32 m0, s58
	v_lshl_add_u64 v[24:25], s[46:47], 0, v[164:165]
	global_load_lds_dwordx4 v[22:23], off
	v_lshl_add_u64 v[22:23], vcc, 0, v[166:167]
	s_mov_b32 m0, s59
	s_nop 0
	global_load_lds_dwordx4 v[22:23], off
	v_lshl_add_u64 v[22:23], s[46:47], 0, v[162:163]
	s_mov_b32 m0, s37
	s_nop 0
	global_load_lds_dwordx4 v[22:23], off
	s_mov_b32 m0, s60
	s_nop 0
	global_load_lds_dwordx4 v[24:25], off
	s_waitcnt vmcnt(8)
	s_waitcnt lgkmcnt(0)
	s_barrier
	s_setprio 1
	s_waitcnt lgkmcnt(0)
	v_mfma_scale_f32_16x16x128_f8f6f4 v[94:97], v[2:9], v[198:205], v[94:97], v234, v238 op_sel_hi:[0,0,0]
	v_mfma_scale_f32_16x16x128_f8f6f4 v[90:93], v[10:17], v[198:205], v[90:93], v234, v238 op_sel_hi:[0,0,0]
	v_mfma_scale_f32_16x16x128_f8f6f4 v[86:89], v[2:9], v[206:213], v[86:89], v234, v238 op_sel_hi:[0,0,0]
	v_mfma_scale_f32_16x16x128_f8f6f4 v[82:85], v[10:17], v[206:213], v[82:85], v234, v238 op_sel_hi:[0,0,0]
	v_mfma_scale_f32_16x16x128_f8f6f4 v[78:81], v[2:9], v[216:223], v[78:81], v234, v238 op_sel_hi:[0,0,0]
	v_mfma_scale_f32_16x16x128_f8f6f4 v[74:77], v[10:17], v[216:223], v[74:77], v234, v238 op_sel_hi:[0,0,0]
	v_mfma_scale_f32_16x16x128_f8f6f4 v[70:73], v[2:9], v[224:231], v[70:73], v234, v238 op_sel_hi:[0,0,0]
	v_mfma_scale_f32_16x16x128_f8f6f4 v[66:69], v[10:17], v[224:231], v[66:69], v234, v238 op_sel_hi:[0,0,0]
	s_setprio 0
	s_setprio 1
	v_mfma_scale_f32_16x16x128_f8f6f4 v[62:65], v[26:33], v[198:205], v[62:65], v234, v238 op_sel_hi:[0,0,0]
	v_mfma_scale_f32_16x16x128_f8f6f4 v[58:61], v[172:179], v[198:205], v[58:61], v234, v238 op_sel_hi:[0,0,0]
	v_mfma_scale_f32_16x16x128_f8f6f4 v[54:57], v[26:33], v[206:213], v[54:57], v234, v238 op_sel_hi:[0,0,0]
	v_mfma_scale_f32_16x16x128_f8f6f4 v[50:53], v[172:179], v[206:213], v[50:53], v234, v238 op_sel_hi:[0,0,0]
	v_mfma_scale_f32_16x16x128_f8f6f4 v[46:49], v[26:33], v[216:223], v[46:49], v234, v238 op_sel_hi:[0,0,0]
	v_mfma_scale_f32_16x16x128_f8f6f4 v[42:45], v[172:179], v[216:223], v[42:45], v234, v238 op_sel_hi:[0,0,0]
	v_mfma_scale_f32_16x16x128_f8f6f4 v[38:41], v[26:33], v[224:231], v[38:41], v234, v238 op_sel_hi:[0,0,0]
	v_mfma_scale_f32_16x16x128_f8f6f4 v[34:37], v[172:179], v[224:231], v[34:37], v234, v238 op_sel_hi:[0,0,0]
	s_setprio 0
	s_barrier
	s_add_u32 s46, s46, 0x20000
	s_addc_u32 s47, s47, 0
	s_mov_b32 m0, s61
	v_lshl_add_u64 v[232:233], s[46:47], 0, v[162:163]
	global_load_lds_dwordx4 v[232:233], off
	v_lshl_add_u64 v[232:233], s[46:47], 0, v[164:165]
	s_mov_b32 m0, s62
	s_nop 0
	global_load_lds_dwordx4 v[232:233], off
	ds_read_b128 v[10:13], v188
	ds_read_b128 v[14:17], v189
	ds_read_b128 v[26:29], v190
	ds_read_b128 v[30:33], v191
	ds_read_b128 v[2:5], v192
	ds_read_b128 v[6:9], v193
	ds_read_b128 v[172:175], v194
	ds_read_b128 v[176:179], v195
	ds_read_b128 v[198:201], v196 offset:32768
	ds_read_b128 v[202:205], v196 offset:33792
	ds_read_b128 v[206:209], v196 offset:34816
	ds_read_b128 v[210:213], v196 offset:35840
	ds_read_b128 v[216:219], v196 offset:36864
	ds_read_b128 v[220:223], v196 offset:37888
	ds_read_b128 v[224:227], v196 offset:38912
	ds_read_b128 v[228:231], v196 offset:39936
	s_waitcnt vmcnt(8)
	s_waitcnt lgkmcnt(0)
	s_barrier
	s_setprio 1
	s_waitcnt lgkmcnt(0)
	v_mfma_scale_f32_16x16x128_f8f6f4 v[158:161], v[10:17], v[198:205], v[158:161], v234, v238 op_sel_hi:[0,0,0]
	v_mfma_scale_f32_16x16x128_f8f6f4 v[154:157], v[26:33], v[198:205], v[154:157], v234, v238 op_sel_hi:[0,0,0]
	v_mfma_scale_f32_16x16x128_f8f6f4 v[150:153], v[10:17], v[206:213], v[150:153], v234, v238 op_sel_hi:[0,0,0]
	v_mfma_scale_f32_16x16x128_f8f6f4 v[146:149], v[26:33], v[206:213], v[146:149], v234, v238 op_sel_hi:[0,0,0]
	v_mfma_scale_f32_16x16x128_f8f6f4 v[142:145], v[10:17], v[216:223], v[142:145], v234, v238 op_sel_hi:[0,0,0]
	v_mfma_scale_f32_16x16x128_f8f6f4 v[138:141], v[26:33], v[216:223], v[138:141], v234, v238 op_sel_hi:[0,0,0]
	v_mfma_scale_f32_16x16x128_f8f6f4 v[134:137], v[10:17], v[224:231], v[134:137], v234, v238 op_sel_hi:[0,0,0]
	v_mfma_scale_f32_16x16x128_f8f6f4 v[130:133], v[26:33], v[224:231], v[130:133], v234, v238 op_sel_hi:[0,0,0]
	s_setprio 0
	s_setprio 1
	v_mfma_scale_f32_16x16x128_f8f6f4 v[126:129], v[2:9], v[198:205], v[126:129], v234, v238 op_sel_hi:[0,0,0]
	v_mfma_scale_f32_16x16x128_f8f6f4 v[122:125], v[172:179], v[198:205], v[122:125], v234, v238 op_sel_hi:[0,0,0]
	v_mfma_scale_f32_16x16x128_f8f6f4 v[118:121], v[2:9], v[206:213], v[118:121], v234, v238 op_sel_hi:[0,0,0]
	v_mfma_scale_f32_16x16x128_f8f6f4 v[114:117], v[172:179], v[206:213], v[114:117], v234, v238 op_sel_hi:[0,0,0]
	v_mfma_scale_f32_16x16x128_f8f6f4 v[110:113], v[2:9], v[216:223], v[110:113], v234, v238 op_sel_hi:[0,0,0]
	v_mfma_scale_f32_16x16x128_f8f6f4 v[106:109], v[172:179], v[216:223], v[106:109], v234, v238 op_sel_hi:[0,0,0]
	v_mfma_scale_f32_16x16x128_f8f6f4 v[102:105], v[2:9], v[224:231], v[102:105], v234, v238 op_sel_hi:[0,0,0]
	v_mfma_scale_f32_16x16x128_f8f6f4 v[98:101], v[172:179], v[224:231], v[98:101], v234, v238 op_sel_hi:[0,0,0]
	s_setprio 0
	s_barrier
	s_mov_b32 m0, s65
	v_lshl_add_u64 v[18:19], v[18:19], 0, s[66:67]
	s_add_u32 s44, s44, 0x20080
	ds_read_b128 v[198:201], v196 offset:49152
	ds_read_b128 v[202:205], v196 offset:50176
	ds_read_b128 v[206:209], v196 offset:51200
	ds_read_b128 v[210:213], v196 offset:52224
	ds_read_b128 v[216:219], v196 offset:53248
	ds_read_b128 v[220:223], v196 offset:54272
	ds_read_b128 v[224:227], v196 offset:55296
	ds_read_b128 v[228:231], v196 offset:56320
	global_load_lds_dwordx4 v[18:19], off
	v_lshl_add_u64 v[18:19], v[20:21], 0, s[66:67]
	s_mov_b32 m0, s68
	s_addc_u32 s45, s45, 0
	global_load_lds_dwordx4 v[18:19], off
	v_lshl_add_u64 v[18:19], s[44:45], 0, v[0:1]
	s_mov_b32 m0, s51
	s_nop 0
	global_load_lds_dwordx4 v[18:19], off
	v_lshl_add_u64 v[18:19], s[44:45], 0, v[166:167]
	s_mov_b32 m0, s4
	s_nop 0
	global_load_lds_dwordx4 v[18:19], off
	v_lshl_add_u64 v[18:19], v[22:23], 0, s[66:67]
	s_mov_b32 m0, s81
	s_nop 0
	global_load_lds_dwordx4 v[18:19], off
	v_lshl_add_u64 v[18:19], v[24:25], 0, s[66:67]
	s_mov_b32 m0, s50
	s_nop 0
	global_load_lds_dwordx4 v[18:19], off
	s_waitcnt vmcnt(8)
	s_waitcnt lgkmcnt(0)
	s_barrier
	s_setprio 1
	s_waitcnt lgkmcnt(0)
	v_mfma_scale_f32_16x16x128_f8f6f4 v[94:97], v[10:17], v[198:205], v[94:97], v234, v238 op_sel_hi:[0,0,0]
	v_mfma_scale_f32_16x16x128_f8f6f4 v[90:93], v[26:33], v[198:205], v[90:93], v234, v238 op_sel_hi:[0,0,0]
	v_mfma_scale_f32_16x16x128_f8f6f4 v[86:89], v[10:17], v[206:213], v[86:89], v234, v238 op_sel_hi:[0,0,0]
	v_mfma_scale_f32_16x16x128_f8f6f4 v[82:85], v[26:33], v[206:213], v[82:85], v234, v238 op_sel_hi:[0,0,0]
	v_mfma_scale_f32_16x16x128_f8f6f4 v[78:81], v[10:17], v[216:223], v[78:81], v234, v238 op_sel_hi:[0,0,0]
	v_mfma_scale_f32_16x16x128_f8f6f4 v[74:77], v[26:33], v[216:223], v[74:77], v234, v238 op_sel_hi:[0,0,0]
	v_mfma_scale_f32_16x16x128_f8f6f4 v[70:73], v[10:17], v[224:231], v[70:73], v234, v238 op_sel_hi:[0,0,0]
	v_mfma_scale_f32_16x16x128_f8f6f4 v[66:69], v[26:33], v[224:231], v[66:69], v234, v238 op_sel_hi:[0,0,0]
	s_setprio 0
	s_setprio 1
	v_mfma_scale_f32_16x16x128_f8f6f4 v[62:65], v[2:9], v[198:205], v[62:65], v234, v238 op_sel_hi:[0,0,0]
	v_mfma_scale_f32_16x16x128_f8f6f4 v[58:61], v[172:179], v[198:205], v[58:61], v234, v238 op_sel_hi:[0,0,0]
	v_mfma_scale_f32_16x16x128_f8f6f4 v[54:57], v[2:9], v[206:213], v[54:57], v234, v238 op_sel_hi:[0,0,0]
	v_mfma_scale_f32_16x16x128_f8f6f4 v[50:53], v[172:179], v[206:213], v[50:53], v234, v238 op_sel_hi:[0,0,0]
	v_mfma_scale_f32_16x16x128_f8f6f4 v[46:49], v[2:9], v[216:223], v[46:49], v234, v238 op_sel_hi:[0,0,0]
	v_mfma_scale_f32_16x16x128_f8f6f4 v[42:45], v[172:179], v[216:223], v[42:45], v234, v238 op_sel_hi:[0,0,0]
	v_mfma_scale_f32_16x16x128_f8f6f4 v[38:41], v[2:9], v[224:231], v[38:41], v234, v238 op_sel_hi:[0,0,0]
	v_mfma_scale_f32_16x16x128_f8f6f4 v[34:37], v[172:179], v[224:231], v[34:37], v234, v238 op_sel_hi:[0,0,0]
	s_setprio 0
	s_barrier
	s_add_i32 s74, s74, 2
	s_add_u32 s42, s42, 0x100
	s_addc_u32 s43, s43, 0
	s_add_u32 s48, s48, 0x100
	s_addc_u32 s49, s49, 0
	s_cmp_gt_u32 s74, 5
	s_cbranch_scc0 .LBB0_2089
	s_and_b64 vcc, exec, s[8:9]
	s_cbranch_vccz .LBB0_2092
	s_barrier
